# L0 norm1: gate-column LDS weight reads software-pipelined 8 deep (counted lgkmcnt)
# speedup vs baseline: 1.0134x; 1.0009x over previous
; DI unsigned pk2(float lo, float hi) { const f32x2 v = {lo, hi}; return __builtin_bit_cast(unsigned, __builtin_convertvector(v, bf16x2_t)); }
; DI float wave_sum(float v) { v += shx<1>(v); v += shx<2>(v); v += shx<4>(v); v += shx<8>(v); v += shx<16>(v); v += shx<32>(v); return v; }
; template <int MODE, bool SB  > DI void norm_phase(const Params& P, const Frame& F, int L, const void* src_, const float* gain, bool combine) {
;     ...
;     for (int row = r_lo + F.wave; row < r_hi; row += NWAVES) {
;         f32x4 v[8];
; #pragma unroll
;         for (int j = 0; j < 8; ++j) { if constexpr (SB) v[j] = (f32x4){bflo(vb[j].x), bfhi(vb[j].x), bflo(vb[j].y), bfhi(vb[j].y)}; else v[j] = vn[j]; }
;         { const int rnx = (row + NWAVES < r_hi) ? row + NWAVES : row;
; #pragma unroll
;           for (int j = 0; j < 8; ++j) { if constexpr (SB) vb[j] = *(const u32x2*)(srcb + (size_t)rnx * D + 4 * F.lane + 256 * j); else vn[j] = *(const f32x4*)(src + (size_t)rnx * D + 4 * F.lane + 256 * j); } }
;         if (MODE == 3 && combine) {
;             const int* SLOT = (const int*)(ws + WS_SLOT); const float* TOPW = (const float*)(ws + WS_TOPW); const bf16* Y = (const bf16*)(ws + WS_T + T_YPERM);
;             const int s1 = SLOT[row * 2], s2 = SLOT[row * 2 + 1]; const float w1 = TOPW[row * 2], w2 = TOPW[row * 2 + 1];
;             u32x2 ya[8], yb[8];
; #pragma unroll
;             for (int j = 0; j < 8; ++j) { ya[j] = *(const u32x2*)(Y + (size_t)s1 * D + 4 * F.lane + 256 * j); yb[j] = *(const u32x2*)(Y + (size_t)s2 * D + 4 * F.lane + 256 * j); }
; #pragma unroll
;             for (int j = 0; j < 8; ++j) { const f32x4 y1 = (f32x4){bflo(ya[j].x), bfhi(ya[j].x), bflo(ya[j].y), bfhi(ya[j].y)}, y2 = (f32x4){bflo(yb[j].x), bfhi(yb[j].x), bflo(yb[j].y), bfhi(yb[j].y)};
;                 v[j] = v[j] + w1 * y1 + w2 * y2;
;                 const u32x2 hb = {pk2(v[j][0], v[j][1]), pk2(v[j][2], v[j][3])}; *(u32x2*)(const_cast<bf16*>(srcb) + (size_t)row * D + 4 * F.lane + 256 * j) = hb;
;                 v[j] = (f32x4){bflo(hb.x), bfhi(hb.x), bflo(hb.y), bfhi(hb.y)}; }
;         }
;         float ss = 0.f;
; #pragma unroll
;         for (int j = 0; j < 8; ++j) ss += (v[j][0] * v[j][0] + v[j][1] * v[j][1]) + (v[j][2] * v[j][2] + v[j][3] * v[j][3]);
;         const float rstd = 1.0f / sqrtf(wave_sum(ss) * (1.0f / D) + EPS);
.LBB0_83:
	s_waitcnt vmcnt(1)
	v_mov_b64_e32 v[90:91], v[38:39]
	s_waitcnt vmcnt(0)
	v_mov_b64_e32 v[94:95], v[34:35]
	v_mov_b64_e32 v[88:89], v[36:37]
	v_mov_b64_e32 v[92:93], v[32:33]
	v_mov_b32_e32 v114, v93
	v_mov_b32_e32 v115, v89
	v_mov_b32_e32 v112, v92
	v_mov_b32_e32 v113, v88
	v_pk_mul_f32 v[114:115], v[114:115], v[114:115]
	v_mov_b32_e32 v188, v95
	v_mov_b32_e32 v189, v91
	v_mov_b64_e32 v[86:87], v[42:43]
	v_pk_fma_f32 v[112:113], v[112:113], v[112:113], v[114:115]
	v_mov_b32_e32 v114, v94
	v_mov_b32_e32 v115, v90
	v_pk_mul_f32 v[188:189], v[188:189], v[188:189]
	v_mov_b64_e32 v[84:85], v[40:41]
	v_pk_fma_f32 v[114:115], v[114:115], v[114:115], v[188:189]
	v_pk_mul_f32 v[188:189], v[84:85], v[84:85]
	v_pk_add_f32 v[112:113], v[112:113], v[114:115]
	v_pk_mul_f32 v[114:115], v[86:87], v[86:87]
	v_mov_b64_e32 v[78:79], v[50:51]
	v_pk_mov_b32 v[190:191], v[188:189], v[114:115] op_sel:[1,0]
	v_mov_b32_e32 v189, v115
	v_mov_b64_e32 v[76:77], v[48:49]
	v_pk_add_f32 v[114:115], v[190:191], v[188:189]
	v_mov_b64_e32 v[82:83], v[46:47]
	v_mul_f32_e32 v111, v76, v76
	v_mul_f32_e32 v188, v77, v77
	v_pk_add_f32 v[112:113], v[112:113], v[112:113] op_sel:[0,1] op_sel_hi:[1,0]
	v_pk_add_f32 v[114:115], v[114:115], v[114:115] op_sel:[0,1] op_sel_hi:[1,0]
	v_mov_b64_e32 v[80:81], v[44:45]
	v_mov_b32_e32 v113, v111
	v_mov_b32_e32 v115, v188
	v_pk_add_f32 v[112:113], v[112:113], v[114:115]
	v_mul_f32_e32 v114, v81, v81
	v_mul_f32_e32 v189, v78, v78
	v_pk_fma_f32 v[114:115], v[80:81], v[80:81], v[114:115] op_sel_hi:[1,1,0]
	v_mul_f32_e32 v188, v83, v83
	v_mul_f32_e32 v190, v79, v79
	v_mov_b32_e32 v115, v189
	v_pk_fma_f32 v[188:189], v[82:83], v[82:83], v[188:189] op_sel_hi:[1,1,0]
	v_mov_b64_e32 v[74:75], v[54:55]
	v_mov_b32_e32 v189, v190
	v_mov_b64_e32 v[72:73], v[52:53]
	v_pk_add_f32 v[114:115], v[114:115], v[188:189]
	v_pk_mul_f32 v[188:189], v[72:73], v[72:73]
	v_pk_add_f32 v[112:113], v[112:113], v[114:115]
	v_pk_mul_f32 v[114:115], v[74:75], v[74:75]
	v_mov_b64_e32 v[66:67], v[62:63]
	v_pk_mov_b32 v[190:191], v[188:189], v[114:115] op_sel:[1,0]
	v_mov_b32_e32 v189, v115
	v_mov_b64_e32 v[64:65], v[60:61]
	v_pk_add_f32 v[114:115], v[190:191], v[188:189]
	v_mov_b64_e32 v[70:71], v[58:59]
	v_mul_f32_e32 v111, v64, v64
	v_mul_f32_e32 v188, v65, v65
	v_pk_add_f32 v[112:113], v[112:113], v[112:113] op_sel:[0,1] op_sel_hi:[1,0]
	v_pk_add_f32 v[114:115], v[114:115], v[114:115] op_sel:[0,1] op_sel_hi:[1,0]
	v_mov_b64_e32 v[68:69], v[56:57]
	v_mov_b32_e32 v113, v111
	v_mov_b32_e32 v115, v188
	v_pk_add_f32 v[112:113], v[112:113], v[114:115]
	v_mul_f32_e32 v114, v69, v69
	v_mul_f32_e32 v189, v66, v66
	v_pk_fma_f32 v[114:115], v[68:69], v[68:69], v[114:115] op_sel_hi:[1,1,0]
	v_mul_f32_e32 v188, v71, v71
	v_mul_f32_e32 v190, v67, v67
	v_mov_b32_e32 v115, v189
	v_pk_fma_f32 v[188:189], v[70:71], v[70:71], v[188:189] op_sel_hi:[1,1,0]
	s_mov_b32 s20, s0
	v_mov_b32_e32 v189, v190
	v_pk_add_f32 v[114:115], v[114:115], v[188:189]
	s_add_i32 s0, s0, 8
	v_pk_add_f32 v[112:113], v[112:113], v[114:115]
	s_cmp_ge_i32 s0, s3
	v_add_f32_e32 v111, v112, v113
	s_cselect_b64 s[22:23], -1, 0
	s_cmp_lt_i32 s0, s3
	v_add_f32_dpp v111, v111, v111 quad_perm:[1,0,3,2] row_mask:0xf bank_mask:0xf bound_ctrl:1
	s_cselect_b32 s20, s0, s20
	s_ashr_i32 s21, s20, 31
	v_add_f32_dpp v111, v111, v111 quad_perm:[2,3,0,1] row_mask:0xf bank_mask:0xf bound_ctrl:1
	ds_swizzle_b32 v112, v111 offset:swizzle(SWAP,4)
	s_lshl_b64 s[20:21], s[20:21], 13
	v_lshl_add_u64 v[48:49], v[96:97], 0, s[20:21]
	v_add_co_u32_e32 v60, vcc, s30, v48
	s_waitcnt lgkmcnt(0)
	v_add_f32_e32 v111, v111, v112
	ds_swizzle_b32 v112, v111 offset:swizzle(SWAP,8)
	v_addc_co_u32_e32 v61, vcc, 0, v49, vcc
	s_mov_b32 s20, 0xf800000
	global_load_dwordx4 v[32:35], v[48:49], off
	global_load_dwordx4 v[36:39], v[48:49], off offset:1024
	global_load_dwordx4 v[40:43], v[48:49], off offset:2048
	global_load_dwordx4 v[44:47], v[48:49], off offset:3072
	s_waitcnt lgkmcnt(0)
	v_add_f32_e32 v111, v111, v112
	ds_swizzle_b32 v112, v111 offset:swizzle(SWAP,16)
	global_load_dwordx4 v[48:51], v[60:61], off
	global_load_dwordx4 v[52:55], v[60:61], off offset:1024
	global_load_dwordx4 v[56:59], v[60:61], off offset:2048
	s_nop 0
	global_load_dwordx4 v[60:63], v[60:61], off offset:3072
	s_waitcnt lgkmcnt(0)
	v_add_f32_e32 v111, v111, v112
	ds_bpermute_b32 v112, v116, v111
	s_waitcnt lgkmcnt(0)
; #define LAS __attribute__((address_space(3)))
; DI unsigned pk2(float lo, float hi) { const f32x2 v = {lo, hi}; return __builtin_bit_cast(unsigned, __builtin_convertvector(v, bf16x2_t)); }
; DI unsigned pk4_fp8(float a, float b, float c, float d) { unsigned w = 0u; w = __builtin_amdgcn_cvt_pk_fp8_f32(a, b, w, false); w = __builtin_amdgcn_cvt_pk_fp8_f32(c, d, w, true); return w; }
; DI float wave_sum(float v) { v += shx<1>(v); v += shx<2>(v); v += shx<4>(v); v += shx<8>(v); v += shx<16>(v); v += shx<32>(v); return v; }
; template <int MODE, bool SB  > DI void norm_phase(const Params& P, const Frame& F, int L, const void* src_, const float* gain, bool combine) {
;     ...
;         const float rstd = 1.0f / sqrtf(wave_sum(ss) * (1.0f / D) + EPS);
; #pragma unroll
;         for (int j = 0; j < 8; ++j) v[j] = v[j] * rstd * g[j];
;         if (MODE == 4) {
; #pragma unroll
;             for (int j = 0; j < 8; ++j) *(f32x4*)(P.out + (size_t)row * D + 4 * F.lane + 256 * j) = v[j];
;         } else if (MODE == 0 || MODE == 2 || (MODE == 3 && L == 1)) {
;             unsigned* o4 = (unsigned*)((unsigned char*)HN + (size_t)row * D) + F.lane; const float hs = (float)(1 << LS_HN);
; #pragma unroll
;             for (int j = 0; j < 8; ++j) o4[64 * j] = pk4_fp8(v[j][0] * hs, v[j][1] * hs, v[j][2] * hs, v[j][3] * hs);
;         } else {
;             unsigned long long* o8 = (unsigned long long*)(HN + (size_t)row * D) + F.lane;
; #pragma unroll
;             for (int j = 0; j < 8; ++j) o8[64 * j] = (unsigned long long)pk2(v[j][0], v[j][1]) | ((unsigned long long)pk2(v[j][2], v[j][3]) << 32);
;         }
;         if (MODE == 1) {
;             float s[16];
; #pragma unroll
;             for (int q = 0; q < 16; ++q) { float t = 0.f;
; #pragma unroll
;                 for (int j = 0; j < 8; ++j) { const f32x4 w = *(const LAS f32x4*)(F.lds + (size_t)(q * D + 256 * j + 4 * F.lane) * 4); t += (v[j][0] * w[0] + v[j][1] * w[1]) + (v[j][2] * w[2] + v[j][3] * w[3]); }
;                 s[q] = t; if ((q & 3) == 3) asm volatile("" ::: "memory"); }
	v_add_f32_e32 v111, v111, v112
	v_fmamk_f32 v111, v111, 0x3a000000, v182
	v_cmp_gt_f32_e32 vcc, s20, v111
	v_mul_f32_e32 v112, 0x4f800000, v111
	s_nop 0
	v_cndmask_b32_e32 v111, v111, v112, vcc
	v_sqrt_f32_e32 v112, v111
	s_nop 0
	v_add_u32_e32 v113, -1, v112
	v_fma_f32 v114, -v113, v112, v111
	v_cmp_ge_f32_e64 s[20:21], 0, v114
	v_add_u32_e32 v114, 1, v112
	s_nop 0
	v_cndmask_b32_e64 v113, v112, v113, s[20:21]
	v_fma_f32 v112, -v114, v112, v111
	v_cmp_lt_f32_e64 s[20:21], 0, v112
	s_nop 1
	v_cndmask_b32_e64 v112, v113, v114, s[20:21]
	v_mul_f32_e32 v113, 0x37800000, v112
	v_cndmask_b32_e32 v112, v112, v113, vcc
	v_cmp_class_f32_e32 vcc, v111, v183
	s_nop 1
	v_cndmask_b32_e32 v111, v112, v111, vcc
	v_div_scale_f32 v112, s[20:21], v111, v111, 1.0
	v_rcp_f32_e32 v113, v112
	s_mov_b32 s20, 0x3d600000
	v_fma_f32 v114, -v112, v113, 1.0
	v_fmac_f32_e32 v113, v114, v113
	v_div_scale_f32 v114, vcc, 1.0, v111, 1.0
	v_mul_f32_e32 v115, v114, v113
	v_fma_f32 v188, -v112, v115, v114
	v_fmac_f32_e32 v115, v188, v113
	v_fma_f32 v112, -v112, v115, v114
	v_div_fmas_f32 v112, v112, v113, v115
	v_div_fixup_f32 v188, v112, v111, 1.0
	v_pk_mul_f32 v[94:95], v[94:95], v[188:189] op_sel_hi:[1,0]
	v_pk_mul_f32 v[88:89], v[88:89], v[188:189] op_sel_hi:[1,0]
	v_pk_mul_f32 v[86:87], v[86:87], v[188:189] op_sel_hi:[1,0]
	v_pk_mul_f32 v[80:81], v[80:81], v[188:189] op_sel_hi:[1,0]
	v_pk_mul_f32 v[78:79], v[78:79], v[188:189] op_sel_hi:[1,0]
	v_pk_mul_f32 v[72:73], v[72:73], v[188:189] op_sel_hi:[1,0]
	v_pk_mul_f32 v[70:71], v[70:71], v[188:189] op_sel_hi:[1,0]
	v_pk_mul_f32 v[64:65], v[64:65], v[188:189] op_sel_hi:[1,0]
	v_pk_mul_f32 v[92:93], v[92:93], v[188:189] op_sel_hi:[1,0]
	v_pk_mul_f32 v[112:113], v[2:3], v[94:95]
	v_pk_mul_f32 v[94:95], v[4:5], v[88:89]
	v_pk_mul_f32 v[88:89], v[10:11], v[86:87]
	v_pk_mul_f32 v[86:87], v[12:13], v[80:81]
	v_pk_mul_f32 v[80:81], v[18:19], v[78:79]
	v_pk_mul_f32 v[78:79], v[20:21], v[72:73]
	v_pk_mul_f32 v[72:73], v[26:27], v[70:71]
	v_pk_mul_f32 v[70:71], v[28:29], v[64:65]
	v_lshl_add_u64 v[64:65], s[54:55], 0, v[108:109]
	v_pk_mul_f32 v[114:115], v[0:1], v[92:93]
	v_pk_mul_f32 v[90:91], v[90:91], v[188:189] op_sel_hi:[1,0]
	v_pk_mul_f32 v[84:85], v[84:85], v[188:189] op_sel_hi:[1,0]
	v_pk_mul_f32 v[82:83], v[82:83], v[188:189] op_sel_hi:[1,0]
	v_pk_mul_f32 v[76:77], v[76:77], v[188:189] op_sel_hi:[1,0]
	v_pk_mul_f32 v[74:75], v[74:75], v[188:189] op_sel_hi:[1,0]
	v_pk_mul_f32 v[68:69], v[68:69], v[188:189] op_sel_hi:[1,0]
	v_pk_mul_f32 v[66:67], v[66:67], v[188:189] op_sel_hi:[1,0]
	v_add_co_u32_e32 v64, vcc, s20, v64
	v_pk_mul_f32 v[92:93], v[6:7], v[90:91]
	v_pk_mul_f32 v[90:91], v[8:9], v[84:85]
	v_pk_mul_f32 v[84:85], v[14:15], v[82:83]
	v_pk_mul_f32 v[82:83], v[16:17], v[76:77]
	v_pk_mul_f32 v[76:77], v[22:23], v[74:75]
	v_pk_mul_f32 v[74:75], v[24:25], v[68:69]
	v_pk_mul_f32 v[68:69], v[30:31], v[66:67]
	v_cvt_pk_bf16_f32 v66, v114, v115
	v_cvt_pk_bf16_f32 v67, v112, v113
	v_addc_co_u32_e32 v65, vcc, 0, v65, vcc
	global_store_dwordx2 v[64:65], v[66:67], off
	v_cvt_pk_bf16_f32 v66, v94, v95
	v_cvt_pk_bf16_f32 v67, v92, v93
	global_store_dwordx2 v[64:65], v[66:67], off offset:512
	v_cvt_pk_bf16_f32 v66, v90, v91
	v_cvt_pk_bf16_f32 v67, v88, v89
	global_store_dwordx2 v[64:65], v[66:67], off offset:1024
	v_cvt_pk_bf16_f32 v66, v86, v87
	v_cvt_pk_bf16_f32 v67, v84, v85
	global_store_dwordx2 v[64:65], v[66:67], off offset:1536
	v_cvt_pk_bf16_f32 v66, v82, v83
	v_cvt_pk_bf16_f32 v67, v80, v81
	global_store_dwordx2 v[64:65], v[66:67], off offset:2048
	v_cvt_pk_bf16_f32 v66, v78, v79
	v_cvt_pk_bf16_f32 v67, v76, v77
	global_store_dwordx2 v[64:65], v[66:67], off offset:2560
	v_cvt_pk_bf16_f32 v66, v74, v75
	v_cvt_pk_bf16_f32 v67, v72, v73
	global_store_dwordx2 v[64:65], v[66:67], off offset:3072
	v_cvt_pk_bf16_f32 v66, v70, v71
	v_cvt_pk_bf16_f32 v67, v68, v69
	global_store_dwordx2 v[64:65], v[66:67], off offset:3584
	ds_read_b128 v[216:219], v117
	ds_read_b128 v[220:223], v117 offset:1024
	ds_read_b128 v[224:227], v117 offset:2048
	ds_read_b128 v[228:231], v117 offset:3072
	ds_read_b128 v[232:235], v117 offset:4096
	ds_read_b128 v[236:239], v117 offset:5120
	ds_read_b128 v[240:243], v117 offset:6144
	ds_read_b128 v[248:251], v117 offset:7168
	s_waitcnt lgkmcnt(7)
	v_mul_f32_e32 v217, v217, v115
	v_fmac_f32_e32 v217, v216, v114
	v_mul_f32_e32 v216, v219, v113
	v_fmac_f32_e32 v216, v218, v112
	v_add_f32_e32 v216, v217, v216
	v_add_f32_e32 v111, 0, v216
	ds_read_b128 v[216:219], v117 offset:8192
	s_waitcnt lgkmcnt(7)
	v_mul_f32_e32 v221, v95, v221
	v_fmac_f32_e32 v221, v94, v220
	v_mul_f32_e32 v220, v93, v223
	v_fmac_f32_e32 v220, v92, v222
	v_add_f32_e32 v220, v221, v220
	v_add_f32_e32 v111, v220, v111
	ds_read_b128 v[220:223], v117 offset:9216
	s_waitcnt lgkmcnt(7)
	v_mul_f32_e32 v225, v91, v225
	v_fmac_f32_e32 v225, v90, v224
	v_mul_f32_e32 v224, v89, v227
	v_fmac_f32_e32 v224, v88, v226
	v_add_f32_e32 v224, v225, v224
	v_add_f32_e32 v111, v224, v111
	ds_read_b128 v[224:227], v117 offset:10240
	s_waitcnt lgkmcnt(7)
	v_mul_f32_e32 v229, v87, v229
	v_fmac_f32_e32 v229, v86, v228
	v_mul_f32_e32 v228, v85, v231
	v_fmac_f32_e32 v228, v84, v230
	v_add_f32_e32 v228, v229, v228
	v_add_f32_e32 v111, v228, v111
	ds_read_b128 v[228:231], v117 offset:11264
	s_waitcnt lgkmcnt(7)
	v_mul_f32_e32 v233, v83, v233
	v_fmac_f32_e32 v233, v82, v232
	v_mul_f32_e32 v232, v81, v235
	v_fmac_f32_e32 v232, v80, v234
	v_add_f32_e32 v232, v233, v232
	v_add_f32_e32 v111, v232, v111
	ds_read_b128 v[232:235], v117 offset:12288
	s_waitcnt lgkmcnt(7)
; #define LAS __attribute__((address_space(3)))
; template <int MODE, bool SB  > DI void norm_phase(const Params& P, const Frame& F, int L, const void* src_, const float* gain, bool combine) {
;     ...
;             for (int q = 0; q < 16; ++q) { float t = 0.f;
; #pragma unroll
;                 for (int j = 0; j < 8; ++j) { const f32x4 w = *(const LAS f32x4*)(F.lds + (size_t)(q * D + 256 * j + 4 * F.lane) * 4); t += (v[j][0] * w[0] + v[j][1] * w[1]) + (v[j][2] * w[2] + v[j][3] * w[3]); }
;                 s[q] = t; if ((q & 3) == 3) asm volatile("" ::: "memory"); }
	v_mul_f32_e32 v237, v79, v237
	v_fmac_f32_e32 v237, v78, v236
	v_mul_f32_e32 v236, v77, v239
	v_fmac_f32_e32 v236, v76, v238
	v_add_f32_e32 v236, v237, v236
	v_add_f32_e32 v111, v236, v111
	ds_read_b128 v[236:239], v117 offset:13312
	s_waitcnt lgkmcnt(7)
	v_mul_f32_e32 v241, v75, v241
	v_fmac_f32_e32 v241, v74, v240
	v_mul_f32_e32 v240, v73, v243
	v_fmac_f32_e32 v240, v72, v242
	v_add_f32_e32 v240, v241, v240
	v_add_f32_e32 v111, v240, v111
	ds_read_b128 v[240:243], v117 offset:14336
	s_waitcnt lgkmcnt(7)
	v_mul_f32_e32 v249, v71, v249
	v_fmac_f32_e32 v249, v70, v248
	v_mul_f32_e32 v248, v69, v251
	v_fmac_f32_e32 v248, v68, v250
	v_add_f32_e32 v248, v249, v248
	v_add_f32_e32 v111, v248, v111
	ds_read_b128 v[248:251], v117 offset:15360
	s_waitcnt lgkmcnt(7)
	v_mul_f32_e32 v217, v115, v217
	v_fmac_f32_e32 v217, v114, v216
	v_mul_f32_e32 v216, v113, v219
	v_fmac_f32_e32 v216, v112, v218
	v_add_f32_e32 v216, v217, v216
	v_add_f32_e32 v188, 0, v216
	ds_read_b128 v[216:219], v117 offset:16384
	s_waitcnt lgkmcnt(7)
	v_mul_f32_e32 v221, v95, v221
	v_fmac_f32_e32 v221, v94, v220
	v_mul_f32_e32 v220, v93, v223
	v_fmac_f32_e32 v220, v92, v222
	v_add_f32_e32 v220, v221, v220
	v_add_f32_e32 v188, v188, v220
	ds_read_b128 v[220:223], v117 offset:17408
	s_waitcnt lgkmcnt(7)
	v_mul_f32_e32 v225, v91, v225
	v_fmac_f32_e32 v225, v90, v224
	v_mul_f32_e32 v224, v89, v227
	v_fmac_f32_e32 v224, v88, v226
	v_add_f32_e32 v224, v225, v224
	v_add_f32_e32 v188, v188, v224
	ds_read_b128 v[224:227], v117 offset:18432
	s_waitcnt lgkmcnt(7)
	v_mul_f32_e32 v229, v87, v229
	v_fmac_f32_e32 v229, v86, v228
	v_mul_f32_e32 v228, v85, v231
	v_fmac_f32_e32 v228, v84, v230
	v_add_f32_e32 v228, v229, v228
	v_add_f32_e32 v188, v188, v228
	ds_read_b128 v[228:231], v117 offset:19456
	s_waitcnt lgkmcnt(7)
	v_mul_f32_e32 v233, v83, v233
	v_fmac_f32_e32 v233, v82, v232
	v_mul_f32_e32 v232, v81, v235
	v_fmac_f32_e32 v232, v80, v234
	v_add_f32_e32 v232, v233, v232
	v_add_f32_e32 v188, v188, v232
	ds_read_b128 v[232:235], v117 offset:20480
	s_waitcnt lgkmcnt(7)
	v_mul_f32_e32 v237, v79, v237
	v_fmac_f32_e32 v237, v78, v236
	v_mul_f32_e32 v236, v77, v239
	v_fmac_f32_e32 v236, v76, v238
	v_add_f32_e32 v236, v237, v236
	v_add_f32_e32 v188, v188, v236
	ds_read_b128 v[236:239], v117 offset:21504
	s_waitcnt lgkmcnt(7)
	v_mul_f32_e32 v241, v75, v241
	v_fmac_f32_e32 v241, v74, v240
	v_mul_f32_e32 v240, v73, v243
	v_fmac_f32_e32 v240, v72, v242
	v_add_f32_e32 v240, v241, v240
	v_add_f32_e32 v188, v188, v240
	ds_read_b128 v[240:243], v117 offset:22528
	s_waitcnt lgkmcnt(7)
	v_mul_f32_e32 v249, v71, v249
	v_fmac_f32_e32 v249, v70, v248
	v_mul_f32_e32 v248, v69, v251
	v_fmac_f32_e32 v248, v68, v250
	v_add_f32_e32 v248, v249, v248
	v_add_f32_e32 v188, v188, v248
	ds_read_b128 v[248:251], v117 offset:23552
	s_waitcnt lgkmcnt(7)
	v_mul_f32_e32 v217, v115, v217
	v_fmac_f32_e32 v217, v114, v216
	v_mul_f32_e32 v216, v113, v219
	v_fmac_f32_e32 v216, v112, v218
	v_add_f32_e32 v216, v217, v216
	v_add_f32_e32 v189, 0, v216
	ds_read_b128 v[216:219], v117 offset:24576
	s_waitcnt lgkmcnt(7)
	v_mul_f32_e32 v221, v95, v221
	v_fmac_f32_e32 v221, v94, v220
	v_mul_f32_e32 v220, v93, v223
	v_fmac_f32_e32 v220, v92, v222
	v_add_f32_e32 v220, v221, v220
	v_add_f32_e32 v189, v189, v220
	ds_read_b128 v[220:223], v117 offset:25600
	s_waitcnt lgkmcnt(7)
	v_mul_f32_e32 v225, v91, v225
	v_fmac_f32_e32 v225, v90, v224
	v_mul_f32_e32 v224, v89, v227
	v_fmac_f32_e32 v224, v88, v226
	v_add_f32_e32 v224, v225, v224
	v_add_f32_e32 v189, v189, v224
	ds_read_b128 v[224:227], v117 offset:26624
	s_waitcnt lgkmcnt(7)
	v_mul_f32_e32 v229, v87, v229
	v_fmac_f32_e32 v229, v86, v228
	v_mul_f32_e32 v228, v85, v231
	v_fmac_f32_e32 v228, v84, v230
	v_add_f32_e32 v228, v229, v228
	v_add_f32_e32 v189, v189, v228
	ds_read_b128 v[228:231], v117 offset:27648
	s_waitcnt lgkmcnt(7)
	v_mul_f32_e32 v233, v83, v233
	v_fmac_f32_e32 v233, v82, v232
	v_mul_f32_e32 v232, v81, v235
	v_fmac_f32_e32 v232, v80, v234
	v_add_f32_e32 v232, v233, v232
	v_add_f32_e32 v189, v189, v232
	ds_read_b128 v[232:235], v117 offset:28672
	s_waitcnt lgkmcnt(7)
	v_mul_f32_e32 v237, v79, v237
	v_fmac_f32_e32 v237, v78, v236
	v_mul_f32_e32 v236, v77, v239
	v_fmac_f32_e32 v236, v76, v238
	v_add_f32_e32 v236, v237, v236
	v_add_f32_e32 v189, v189, v236
	ds_read_b128 v[236:239], v117 offset:29696
	s_waitcnt lgkmcnt(7)
	v_mul_f32_e32 v241, v75, v241
	v_fmac_f32_e32 v241, v74, v240
	v_mul_f32_e32 v240, v73, v243
	v_fmac_f32_e32 v240, v72, v242
	v_add_f32_e32 v240, v241, v240
	v_add_f32_e32 v189, v189, v240
	ds_read_b128 v[240:243], v117 offset:30720
	s_waitcnt lgkmcnt(7)
	v_mul_f32_e32 v249, v71, v249
	v_fmac_f32_e32 v249, v70, v248
	v_mul_f32_e32 v248, v69, v251
	v_fmac_f32_e32 v248, v68, v250
	v_add_f32_e32 v248, v249, v248
	v_add_f32_e32 v189, v189, v248
	ds_read_b128 v[248:251], v117 offset:31744
	s_waitcnt lgkmcnt(7)
	v_mul_f32_e32 v217, v115, v217
	v_fmac_f32_e32 v217, v114, v216
	v_mul_f32_e32 v216, v113, v219
	v_fmac_f32_e32 v216, v112, v218
	v_add_f32_e32 v216, v217, v216
	v_add_f32_e32 v190, 0, v216
	ds_read_b128 v[216:219], v117 offset:32768
	s_waitcnt lgkmcnt(7)
	v_mul_f32_e32 v221, v95, v221
	v_fmac_f32_e32 v221, v94, v220
	v_mul_f32_e32 v220, v93, v223
	v_fmac_f32_e32 v220, v92, v222
	v_add_f32_e32 v220, v221, v220
	v_add_f32_e32 v190, v190, v220
	ds_read_b128 v[220:223], v117 offset:33792
	s_waitcnt lgkmcnt(7)
	v_mul_f32_e32 v225, v91, v225
	v_fmac_f32_e32 v225, v90, v224
	v_mul_f32_e32 v224, v89, v227
	v_fmac_f32_e32 v224, v88, v226
	v_add_f32_e32 v224, v225, v224
	v_add_f32_e32 v190, v190, v224
	ds_read_b128 v[224:227], v117 offset:34816
	s_waitcnt lgkmcnt(7)
; #define LAS __attribute__((address_space(3)))
; template <int MODE, bool SB  > DI void norm_phase(const Params& P, const Frame& F, int L, const void* src_, const float* gain, bool combine) {
;     ...
;             for (int q = 0; q < 16; ++q) { float t = 0.f;
; #pragma unroll
;                 for (int j = 0; j < 8; ++j) { const f32x4 w = *(const LAS f32x4*)(F.lds + (size_t)(q * D + 256 * j + 4 * F.lane) * 4); t += (v[j][0] * w[0] + v[j][1] * w[1]) + (v[j][2] * w[2] + v[j][3] * w[3]); }
;                 s[q] = t; if ((q & 3) == 3) asm volatile("" ::: "memory"); }
	v_mul_f32_e32 v229, v87, v229
	v_fmac_f32_e32 v229, v86, v228
	v_mul_f32_e32 v228, v85, v231
	v_fmac_f32_e32 v228, v84, v230
	v_add_f32_e32 v228, v229, v228
	v_add_f32_e32 v190, v190, v228
	ds_read_b128 v[228:231], v117 offset:35840
	s_waitcnt lgkmcnt(7)
	v_mul_f32_e32 v233, v83, v233
	v_fmac_f32_e32 v233, v82, v232
	v_mul_f32_e32 v232, v81, v235
	v_fmac_f32_e32 v232, v80, v234
	v_add_f32_e32 v232, v233, v232
	v_add_f32_e32 v190, v190, v232
	ds_read_b128 v[232:235], v117 offset:36864
	s_waitcnt lgkmcnt(7)
	v_mul_f32_e32 v237, v79, v237
	v_fmac_f32_e32 v237, v78, v236
	v_mul_f32_e32 v236, v77, v239
	v_fmac_f32_e32 v236, v76, v238
	v_add_f32_e32 v236, v237, v236
	v_add_f32_e32 v190, v190, v236
	ds_read_b128 v[236:239], v117 offset:37888
	s_waitcnt lgkmcnt(7)
	v_mul_f32_e32 v241, v75, v241
	v_fmac_f32_e32 v241, v74, v240
	v_mul_f32_e32 v240, v73, v243
	v_fmac_f32_e32 v240, v72, v242
	v_add_f32_e32 v240, v241, v240
	v_add_f32_e32 v190, v190, v240
	ds_read_b128 v[240:243], v117 offset:38912
	s_waitcnt lgkmcnt(7)
	v_mul_f32_e32 v249, v71, v249
	v_fmac_f32_e32 v249, v70, v248
	v_mul_f32_e32 v248, v69, v251
	v_fmac_f32_e32 v248, v68, v250
	v_add_f32_e32 v248, v249, v248
	v_add_f32_e32 v190, v190, v248
	ds_read_b128 v[248:251], v117 offset:39936
	s_waitcnt lgkmcnt(7)
	v_mul_f32_e32 v217, v115, v217
	v_fmac_f32_e32 v217, v114, v216
	v_mul_f32_e32 v216, v113, v219
	v_fmac_f32_e32 v216, v112, v218
	v_add_f32_e32 v216, v217, v216
	v_add_f32_e32 v191, 0, v216
	ds_read_b128 v[216:219], v117 offset:40960
	s_waitcnt lgkmcnt(7)
	v_mul_f32_e32 v221, v95, v221
	v_fmac_f32_e32 v221, v94, v220
	v_mul_f32_e32 v220, v93, v223
	v_fmac_f32_e32 v220, v92, v222
	v_add_f32_e32 v220, v221, v220
	v_add_f32_e32 v191, v191, v220
	ds_read_b128 v[220:223], v117 offset:41984
	s_waitcnt lgkmcnt(7)
	v_mul_f32_e32 v225, v91, v225
	v_fmac_f32_e32 v225, v90, v224
	v_mul_f32_e32 v224, v89, v227
	v_fmac_f32_e32 v224, v88, v226
	v_add_f32_e32 v224, v225, v224
	v_add_f32_e32 v191, v191, v224
	ds_read_b128 v[224:227], v117 offset:43008
	s_waitcnt lgkmcnt(7)
	v_mul_f32_e32 v229, v87, v229
	v_fmac_f32_e32 v229, v86, v228
	v_mul_f32_e32 v228, v85, v231
	v_fmac_f32_e32 v228, v84, v230
	v_add_f32_e32 v228, v229, v228
	v_add_f32_e32 v191, v191, v228
	ds_read_b128 v[228:231], v117 offset:44032
	s_waitcnt lgkmcnt(7)
	v_mul_f32_e32 v233, v83, v233
	v_fmac_f32_e32 v233, v82, v232
	v_mul_f32_e32 v232, v81, v235
	v_fmac_f32_e32 v232, v80, v234
	v_add_f32_e32 v232, v233, v232
	v_add_f32_e32 v191, v191, v232
	ds_read_b128 v[232:235], v117 offset:45056
	s_waitcnt lgkmcnt(7)
	v_mul_f32_e32 v237, v79, v237
	v_fmac_f32_e32 v237, v78, v236
	v_mul_f32_e32 v236, v77, v239
	v_fmac_f32_e32 v236, v76, v238
	v_add_f32_e32 v236, v237, v236
	v_add_f32_e32 v191, v191, v236
	ds_read_b128 v[236:239], v117 offset:46080
	s_waitcnt lgkmcnt(7)
	v_mul_f32_e32 v241, v75, v241
	v_fmac_f32_e32 v241, v74, v240
	v_mul_f32_e32 v240, v73, v243
	v_fmac_f32_e32 v240, v72, v242
	v_add_f32_e32 v240, v241, v240
	v_add_f32_e32 v191, v191, v240
	ds_read_b128 v[240:243], v117 offset:47104
	s_waitcnt lgkmcnt(7)
	v_mul_f32_e32 v249, v71, v249
	v_fmac_f32_e32 v249, v70, v248
	v_mul_f32_e32 v248, v69, v251
	v_fmac_f32_e32 v248, v68, v250
	v_add_f32_e32 v248, v249, v248
	v_add_f32_e32 v191, v191, v248
	ds_read_b128 v[248:251], v117 offset:48128
	s_waitcnt lgkmcnt(7)
	v_mul_f32_e32 v217, v115, v217
	v_fmac_f32_e32 v217, v114, v216
	v_mul_f32_e32 v216, v113, v219
	v_fmac_f32_e32 v216, v112, v218
	v_add_f32_e32 v216, v217, v216
	v_add_f32_e32 v192, 0, v216
	ds_read_b128 v[216:219], v117 offset:49152
	s_waitcnt lgkmcnt(7)
	v_mul_f32_e32 v221, v95, v221
	v_fmac_f32_e32 v221, v94, v220
	v_mul_f32_e32 v220, v93, v223
	v_fmac_f32_e32 v220, v92, v222
	v_add_f32_e32 v220, v221, v220
	v_add_f32_e32 v192, v192, v220
	ds_read_b128 v[220:223], v117 offset:50176
	s_waitcnt lgkmcnt(7)
	v_mul_f32_e32 v225, v91, v225
	v_fmac_f32_e32 v225, v90, v224
	v_mul_f32_e32 v224, v89, v227
	v_fmac_f32_e32 v224, v88, v226
	v_add_f32_e32 v224, v225, v224
	v_add_f32_e32 v192, v192, v224
	ds_read_b128 v[224:227], v117 offset:51200
	s_waitcnt lgkmcnt(7)
	v_mul_f32_e32 v229, v87, v229
	v_fmac_f32_e32 v229, v86, v228
	v_mul_f32_e32 v228, v85, v231
	v_fmac_f32_e32 v228, v84, v230
	v_add_f32_e32 v228, v229, v228
	v_add_f32_e32 v192, v192, v228
	ds_read_b128 v[228:231], v117 offset:52224
	s_waitcnt lgkmcnt(7)
	v_mul_f32_e32 v233, v83, v233
	v_fmac_f32_e32 v233, v82, v232
	v_mul_f32_e32 v232, v81, v235
	v_fmac_f32_e32 v232, v80, v234
	v_add_f32_e32 v232, v233, v232
	v_add_f32_e32 v192, v192, v232
	ds_read_b128 v[232:235], v117 offset:53248
	s_waitcnt lgkmcnt(7)
	v_mul_f32_e32 v237, v79, v237
	v_fmac_f32_e32 v237, v78, v236
	v_mul_f32_e32 v236, v77, v239
	v_fmac_f32_e32 v236, v76, v238
	v_add_f32_e32 v236, v237, v236
	v_add_f32_e32 v192, v192, v236
	ds_read_b128 v[236:239], v117 offset:54272
	s_waitcnt lgkmcnt(7)
	v_mul_f32_e32 v241, v75, v241
	v_fmac_f32_e32 v241, v74, v240
	v_mul_f32_e32 v240, v73, v243
	v_fmac_f32_e32 v240, v72, v242
	v_add_f32_e32 v240, v241, v240
	v_add_f32_e32 v192, v192, v240
	ds_read_b128 v[240:243], v117 offset:55296
	s_waitcnt lgkmcnt(7)
	v_mul_f32_e32 v249, v71, v249
	v_fmac_f32_e32 v249, v70, v248
	v_mul_f32_e32 v248, v69, v251
	v_fmac_f32_e32 v248, v68, v250
	v_add_f32_e32 v248, v249, v248
	v_add_f32_e32 v193, v192, v248
	ds_read_b128 v[248:251], v117 offset:56320
	s_waitcnt lgkmcnt(7)
	v_mul_f32_e32 v217, v115, v217
	v_fmac_f32_e32 v217, v114, v216
	v_mul_f32_e32 v216, v113, v219
	v_fmac_f32_e32 v216, v112, v218
	v_add_f32_e32 v216, v217, v216
	v_add_f32_e32 v192, 0, v216
	ds_read_b128 v[216:219], v117 offset:57344
	s_waitcnt lgkmcnt(7)
; #define LAS __attribute__((address_space(3)))
; template <int MODE, bool SB  > DI void norm_phase(const Params& P, const Frame& F, int L, const void* src_, const float* gain, bool combine) {
;     ...
;             for (int q = 0; q < 16; ++q) { float t = 0.f;
; #pragma unroll
;                 for (int j = 0; j < 8; ++j) { const f32x4 w = *(const LAS f32x4*)(F.lds + (size_t)(q * D + 256 * j + 4 * F.lane) * 4); t += (v[j][0] * w[0] + v[j][1] * w[1]) + (v[j][2] * w[2] + v[j][3] * w[3]); }
;                 s[q] = t; if ((q & 3) == 3) asm volatile("" ::: "memory"); }
	v_mul_f32_e32 v221, v95, v221
	v_fmac_f32_e32 v221, v94, v220
	v_mul_f32_e32 v220, v93, v223
	v_fmac_f32_e32 v220, v92, v222
	v_add_f32_e32 v220, v221, v220
	v_add_f32_e32 v192, v192, v220
	ds_read_b128 v[220:223], v117 offset:58368
	s_waitcnt lgkmcnt(7)
	v_mul_f32_e32 v225, v91, v225
	v_fmac_f32_e32 v225, v90, v224
	v_mul_f32_e32 v224, v89, v227
	v_fmac_f32_e32 v224, v88, v226
	v_add_f32_e32 v224, v225, v224
	v_add_f32_e32 v192, v192, v224
	ds_read_b128 v[224:227], v117 offset:59392
	s_waitcnt lgkmcnt(7)
	v_mul_f32_e32 v229, v87, v229
	v_fmac_f32_e32 v229, v86, v228
	v_mul_f32_e32 v228, v85, v231
	v_fmac_f32_e32 v228, v84, v230
	v_add_f32_e32 v228, v229, v228
	v_add_f32_e32 v192, v192, v228
	ds_read_b128 v[228:231], v117 offset:60416
	s_waitcnt lgkmcnt(7)
	v_mul_f32_e32 v233, v83, v233
	v_fmac_f32_e32 v233, v82, v232
	v_mul_f32_e32 v232, v81, v235
	v_fmac_f32_e32 v232, v80, v234
	v_add_f32_e32 v232, v233, v232
	v_add_f32_e32 v192, v192, v232
	ds_read_b128 v[232:235], v117 offset:61440
	s_waitcnt lgkmcnt(7)
	v_mul_f32_e32 v237, v79, v237
	v_fmac_f32_e32 v237, v78, v236
	v_mul_f32_e32 v236, v77, v239
	v_fmac_f32_e32 v236, v76, v238
	v_add_f32_e32 v236, v237, v236
	v_add_f32_e32 v192, v192, v236
	ds_read_b128 v[236:239], v117 offset:62464
	s_waitcnt lgkmcnt(7)
	v_mul_f32_e32 v241, v75, v241
	v_fmac_f32_e32 v241, v74, v240
	v_mul_f32_e32 v240, v73, v243
	v_fmac_f32_e32 v240, v72, v242
	v_add_f32_e32 v240, v241, v240
	v_add_f32_e32 v192, v192, v240
	ds_read_b128 v[240:243], v117 offset:63488
	s_waitcnt lgkmcnt(7)
	v_mul_f32_e32 v249, v71, v249
	v_fmac_f32_e32 v249, v70, v248
	v_mul_f32_e32 v248, v69, v251
	v_fmac_f32_e32 v248, v68, v250
	v_add_f32_e32 v248, v249, v248
	v_add_f32_e32 v194, v192, v248
	ds_read_b128 v[248:251], v117 offset:64512
	s_waitcnt lgkmcnt(7)
	v_mul_f32_e32 v217, v115, v217
	v_fmac_f32_e32 v217, v114, v216
	v_mul_f32_e32 v216, v113, v219
	v_fmac_f32_e32 v216, v112, v218
	v_add_f32_e32 v216, v217, v216
	v_add_f32_e32 v192, 0, v216
	ds_read_b128 v[216:219], v118
	s_waitcnt lgkmcnt(7)
	v_mul_f32_e32 v221, v95, v221
	v_fmac_f32_e32 v221, v94, v220
	v_mul_f32_e32 v220, v93, v223
	v_fmac_f32_e32 v220, v92, v222
	v_add_f32_e32 v220, v221, v220
	v_add_f32_e32 v192, v192, v220
	ds_read_b128 v[220:223], v119
	s_waitcnt lgkmcnt(7)
	v_mul_f32_e32 v225, v91, v225
	v_fmac_f32_e32 v225, v90, v224
	v_mul_f32_e32 v224, v89, v227
	v_fmac_f32_e32 v224, v88, v226
	v_add_f32_e32 v224, v225, v224
	v_add_f32_e32 v192, v192, v224
	ds_read_b128 v[224:227], v120
	s_waitcnt lgkmcnt(7)
	v_mul_f32_e32 v229, v87, v229
	v_fmac_f32_e32 v229, v86, v228
	v_mul_f32_e32 v228, v85, v231
	v_fmac_f32_e32 v228, v84, v230
	v_add_f32_e32 v228, v229, v228
	v_add_f32_e32 v192, v192, v228
	ds_read_b128 v[228:231], v121
	s_waitcnt lgkmcnt(7)
	v_mul_f32_e32 v233, v83, v233
	v_fmac_f32_e32 v233, v82, v232
	v_mul_f32_e32 v232, v81, v235
	v_fmac_f32_e32 v232, v80, v234
	v_add_f32_e32 v232, v233, v232
	v_add_f32_e32 v192, v192, v232
	ds_read_b128 v[232:235], v122
	s_waitcnt lgkmcnt(7)
	v_mul_f32_e32 v237, v79, v237
	v_fmac_f32_e32 v237, v78, v236
	v_mul_f32_e32 v236, v77, v239
	v_fmac_f32_e32 v236, v76, v238
	v_add_f32_e32 v236, v237, v236
	v_add_f32_e32 v192, v192, v236
	ds_read_b128 v[236:239], v123
	s_waitcnt lgkmcnt(7)
	v_mul_f32_e32 v241, v75, v241
	v_fmac_f32_e32 v241, v74, v240
	v_mul_f32_e32 v240, v73, v243
	v_fmac_f32_e32 v240, v72, v242
	v_add_f32_e32 v240, v241, v240
	v_add_f32_e32 v192, v192, v240
	ds_read_b128 v[240:243], v124
	s_waitcnt lgkmcnt(7)
	v_mul_f32_e32 v249, v71, v249
	v_fmac_f32_e32 v249, v70, v248
	v_mul_f32_e32 v248, v69, v251
	v_fmac_f32_e32 v248, v68, v250
	v_add_f32_e32 v248, v249, v248
	v_add_f32_e32 v195, v192, v248
	ds_read_b128 v[248:251], v125
	s_waitcnt lgkmcnt(7)
	v_mul_f32_e32 v217, v115, v217
	v_fmac_f32_e32 v217, v114, v216
	v_mul_f32_e32 v216, v113, v219
	v_fmac_f32_e32 v216, v112, v218
	v_add_f32_e32 v216, v217, v216
	v_add_f32_e32 v192, 0, v216
	ds_read_b128 v[216:219], v126
	s_waitcnt lgkmcnt(7)
	v_mul_f32_e32 v221, v95, v221
	v_fmac_f32_e32 v221, v94, v220
	v_mul_f32_e32 v220, v93, v223
	v_fmac_f32_e32 v220, v92, v222
	v_add_f32_e32 v220, v221, v220
	v_add_f32_e32 v192, v192, v220
	ds_read_b128 v[220:223], v127
	s_waitcnt lgkmcnt(7)
	v_mul_f32_e32 v225, v91, v225
	v_fmac_f32_e32 v225, v90, v224
	v_mul_f32_e32 v224, v89, v227
	v_fmac_f32_e32 v224, v88, v226
	v_add_f32_e32 v224, v225, v224
	v_add_f32_e32 v192, v192, v224
	ds_read_b128 v[224:227], v128
	s_waitcnt lgkmcnt(7)
	v_mul_f32_e32 v229, v87, v229
	v_fmac_f32_e32 v229, v86, v228
	v_mul_f32_e32 v228, v85, v231
	v_fmac_f32_e32 v228, v84, v230
	v_add_f32_e32 v228, v229, v228
	v_add_f32_e32 v192, v192, v228
	ds_read_b128 v[228:231], v129
	s_waitcnt lgkmcnt(7)
	v_mul_f32_e32 v233, v83, v233
	v_fmac_f32_e32 v233, v82, v232
	v_mul_f32_e32 v232, v81, v235
	v_fmac_f32_e32 v232, v80, v234
	v_add_f32_e32 v232, v233, v232
	v_add_f32_e32 v192, v192, v232
	ds_read_b128 v[232:235], v130
	s_waitcnt lgkmcnt(7)
	v_mul_f32_e32 v237, v79, v237
	v_fmac_f32_e32 v237, v78, v236
	v_mul_f32_e32 v236, v77, v239
	v_fmac_f32_e32 v236, v76, v238
	v_add_f32_e32 v236, v237, v236
	v_add_f32_e32 v192, v192, v236
	ds_read_b128 v[236:239], v131
	s_waitcnt lgkmcnt(7)
	v_mul_f32_e32 v241, v75, v241
	v_fmac_f32_e32 v241, v74, v240
	v_mul_f32_e32 v240, v73, v243
	v_fmac_f32_e32 v240, v72, v242
	v_add_f32_e32 v240, v241, v240
	v_add_f32_e32 v192, v192, v240
	ds_read_b128 v[240:243], v132
	s_waitcnt lgkmcnt(7)
	v_mul_f32_e32 v249, v71, v249
	v_fmac_f32_e32 v249, v70, v248
	v_mul_f32_e32 v248, v69, v251
	v_fmac_f32_e32 v248, v68, v250
	v_add_f32_e32 v248, v249, v248
	v_add_f32_e32 v196, v192, v248
	ds_read_b128 v[248:251], v133
	s_waitcnt lgkmcnt(7)
; #define LAS __attribute__((address_space(3)))
; template <int MODE, bool SB  > DI void norm_phase(const Params& P, const Frame& F, int L, const void* src_, const float* gain, bool combine) {
;     ...
;             for (int q = 0; q < 16; ++q) { float t = 0.f;
; #pragma unroll
;                 for (int j = 0; j < 8; ++j) { const f32x4 w = *(const LAS f32x4*)(F.lds + (size_t)(q * D + 256 * j + 4 * F.lane) * 4); t += (v[j][0] * w[0] + v[j][1] * w[1]) + (v[j][2] * w[2] + v[j][3] * w[3]); }
;                 s[q] = t; if ((q & 3) == 3) asm volatile("" ::: "memory"); }
	v_mul_f32_e32 v217, v115, v217
	v_fmac_f32_e32 v217, v114, v216
	v_mul_f32_e32 v216, v113, v219
	v_fmac_f32_e32 v216, v112, v218
	v_add_f32_e32 v216, v217, v216
	v_add_f32_e32 v192, 0, v216
	ds_read_b128 v[216:219], v134
	s_waitcnt lgkmcnt(7)
	v_mul_f32_e32 v221, v95, v221
	v_fmac_f32_e32 v221, v94, v220
	v_mul_f32_e32 v220, v93, v223
	v_fmac_f32_e32 v220, v92, v222
	v_add_f32_e32 v220, v221, v220
	v_add_f32_e32 v192, v192, v220
	ds_read_b128 v[220:223], v135
	s_waitcnt lgkmcnt(7)
	v_mul_f32_e32 v225, v91, v225
	v_fmac_f32_e32 v225, v90, v224
	v_mul_f32_e32 v224, v89, v227
	v_fmac_f32_e32 v224, v88, v226
	v_add_f32_e32 v224, v225, v224
	v_add_f32_e32 v192, v192, v224
	ds_read_b128 v[224:227], v136
	s_waitcnt lgkmcnt(7)
	v_mul_f32_e32 v229, v87, v229
	v_fmac_f32_e32 v229, v86, v228
	v_mul_f32_e32 v228, v85, v231
	v_fmac_f32_e32 v228, v84, v230
	v_add_f32_e32 v228, v229, v228
	v_add_f32_e32 v192, v192, v228
	ds_read_b128 v[228:231], v137
	s_waitcnt lgkmcnt(7)
	v_mul_f32_e32 v233, v83, v233
	v_fmac_f32_e32 v233, v82, v232
	v_mul_f32_e32 v232, v81, v235
	v_fmac_f32_e32 v232, v80, v234
	v_add_f32_e32 v232, v233, v232
	v_add_f32_e32 v192, v192, v232
	ds_read_b128 v[232:235], v138
	s_waitcnt lgkmcnt(7)
	v_mul_f32_e32 v237, v79, v237
	v_fmac_f32_e32 v237, v78, v236
	v_mul_f32_e32 v236, v77, v239
	v_fmac_f32_e32 v236, v76, v238
	v_add_f32_e32 v236, v237, v236
	v_add_f32_e32 v192, v192, v236
	ds_read_b128 v[236:239], v139
	s_waitcnt lgkmcnt(7)
	v_mul_f32_e32 v241, v75, v241
	v_fmac_f32_e32 v241, v74, v240
	v_mul_f32_e32 v240, v73, v243
	v_fmac_f32_e32 v240, v72, v242
	v_add_f32_e32 v240, v241, v240
	v_add_f32_e32 v192, v192, v240
	ds_read_b128 v[240:243], v140
	s_waitcnt lgkmcnt(7)
	v_mul_f32_e32 v249, v71, v249
	v_fmac_f32_e32 v249, v70, v248
	v_mul_f32_e32 v248, v69, v251
	v_fmac_f32_e32 v248, v68, v250
	v_add_f32_e32 v248, v249, v248
	v_add_f32_e32 v197, v192, v248
	ds_read_b128 v[248:251], v141
	s_waitcnt lgkmcnt(7)
	v_mul_f32_e32 v217, v115, v217
	v_fmac_f32_e32 v217, v114, v216
	v_mul_f32_e32 v216, v113, v219
	v_fmac_f32_e32 v216, v112, v218
	v_add_f32_e32 v216, v217, v216
	v_add_f32_e32 v192, 0, v216
	ds_read_b128 v[216:219], v142
	s_waitcnt lgkmcnt(7)
	v_mul_f32_e32 v221, v95, v221
	v_fmac_f32_e32 v221, v94, v220
	v_mul_f32_e32 v220, v93, v223
	v_fmac_f32_e32 v220, v92, v222
	v_add_f32_e32 v220, v221, v220
	v_add_f32_e32 v192, v192, v220
	ds_read_b128 v[220:223], v143
	s_waitcnt lgkmcnt(7)
	v_mul_f32_e32 v225, v91, v225
	v_fmac_f32_e32 v225, v90, v224
	v_mul_f32_e32 v224, v89, v227
	v_fmac_f32_e32 v224, v88, v226
	v_add_f32_e32 v224, v225, v224
	v_add_f32_e32 v192, v192, v224
	ds_read_b128 v[224:227], v144
	s_waitcnt lgkmcnt(7)
	v_mul_f32_e32 v229, v87, v229
	v_fmac_f32_e32 v229, v86, v228
	v_mul_f32_e32 v228, v85, v231
	v_fmac_f32_e32 v228, v84, v230
	v_add_f32_e32 v228, v229, v228
	v_add_f32_e32 v192, v192, v228
	ds_read_b128 v[228:231], v145
	s_waitcnt lgkmcnt(7)
	v_mul_f32_e32 v233, v83, v233
	v_fmac_f32_e32 v233, v82, v232
	v_mul_f32_e32 v232, v81, v235
	v_fmac_f32_e32 v232, v80, v234
	v_add_f32_e32 v232, v233, v232
	v_add_f32_e32 v192, v192, v232
	ds_read_b128 v[232:235], v146
	s_waitcnt lgkmcnt(7)
	v_mul_f32_e32 v237, v79, v237
	v_fmac_f32_e32 v237, v78, v236
	v_mul_f32_e32 v236, v77, v239
	v_fmac_f32_e32 v236, v76, v238
	v_add_f32_e32 v236, v237, v236
	v_add_f32_e32 v192, v192, v236
	ds_read_b128 v[236:239], v147
	s_waitcnt lgkmcnt(7)
	v_mul_f32_e32 v241, v75, v241
	v_fmac_f32_e32 v241, v74, v240
	v_mul_f32_e32 v240, v73, v243
	v_fmac_f32_e32 v240, v72, v242
	v_add_f32_e32 v240, v241, v240
	v_add_f32_e32 v192, v192, v240
	ds_read_b128 v[240:243], v148
	s_waitcnt lgkmcnt(7)
	v_mul_f32_e32 v249, v71, v249
	v_fmac_f32_e32 v249, v70, v248
	v_mul_f32_e32 v248, v69, v251
	v_fmac_f32_e32 v248, v68, v250
	v_add_f32_e32 v248, v249, v248
	v_add_f32_e32 v198, v192, v248
	ds_read_b128 v[248:251], v149
	s_waitcnt lgkmcnt(7)
	v_mul_f32_e32 v217, v115, v217
	v_fmac_f32_e32 v217, v114, v216
	v_mul_f32_e32 v216, v113, v219
	v_fmac_f32_e32 v216, v112, v218
	v_add_f32_e32 v216, v217, v216
	v_add_f32_e32 v192, 0, v216
	ds_read_b128 v[216:219], v150
	s_waitcnt lgkmcnt(7)
	v_mul_f32_e32 v221, v95, v221
	v_fmac_f32_e32 v221, v94, v220
	v_mul_f32_e32 v220, v93, v223
	v_fmac_f32_e32 v220, v92, v222
	v_add_f32_e32 v220, v221, v220
	v_add_f32_e32 v192, v192, v220
	ds_read_b128 v[220:223], v151
	s_waitcnt lgkmcnt(7)
	v_mul_f32_e32 v225, v91, v225
	v_fmac_f32_e32 v225, v90, v224
	v_mul_f32_e32 v224, v89, v227
	v_fmac_f32_e32 v224, v88, v226
	v_add_f32_e32 v224, v225, v224
	v_add_f32_e32 v192, v192, v224
	ds_read_b128 v[224:227], v152
	s_waitcnt lgkmcnt(7)
	v_mul_f32_e32 v229, v87, v229
	v_fmac_f32_e32 v229, v86, v228
	v_mul_f32_e32 v228, v85, v231
	v_fmac_f32_e32 v228, v84, v230
	v_add_f32_e32 v228, v229, v228
	v_add_f32_e32 v192, v192, v228
	ds_read_b128 v[228:231], v153
	s_waitcnt lgkmcnt(7)
	v_mul_f32_e32 v233, v83, v233
	v_fmac_f32_e32 v233, v82, v232
	v_mul_f32_e32 v232, v81, v235
	v_fmac_f32_e32 v232, v80, v234
	v_add_f32_e32 v232, v233, v232
	v_add_f32_e32 v192, v192, v232
	ds_read_b128 v[232:235], v154
	s_waitcnt lgkmcnt(7)
	v_mul_f32_e32 v237, v79, v237
	v_fmac_f32_e32 v237, v78, v236
	v_mul_f32_e32 v236, v77, v239
	v_fmac_f32_e32 v236, v76, v238
	v_add_f32_e32 v236, v237, v236
	v_add_f32_e32 v192, v192, v236
	ds_read_b128 v[236:239], v155
	s_waitcnt lgkmcnt(7)
	v_mul_f32_e32 v241, v75, v241
	v_fmac_f32_e32 v241, v74, v240
	v_mul_f32_e32 v240, v73, v243
	v_fmac_f32_e32 v240, v72, v242
	v_add_f32_e32 v240, v241, v240
	v_add_f32_e32 v192, v192, v240
	ds_read_b128 v[240:243], v156
	s_waitcnt lgkmcnt(7)
; #define LAS __attribute__((address_space(3)))
; template <int MODE, bool SB  > DI void norm_phase(const Params& P, const Frame& F, int L, const void* src_, const float* gain, bool combine) {
;     ...
;             for (int q = 0; q < 16; ++q) { float t = 0.f;
; #pragma unroll
;                 for (int j = 0; j < 8; ++j) { const f32x4 w = *(const LAS f32x4*)(F.lds + (size_t)(q * D + 256 * j + 4 * F.lane) * 4); t += (v[j][0] * w[0] + v[j][1] * w[1]) + (v[j][2] * w[2] + v[j][3] * w[3]); }
;                 s[q] = t; if ((q & 3) == 3) asm volatile("" ::: "memory"); }
	v_mul_f32_e32 v249, v71, v249
	v_fmac_f32_e32 v249, v70, v248
	v_mul_f32_e32 v248, v69, v251
	v_fmac_f32_e32 v248, v68, v250
	v_add_f32_e32 v248, v249, v248
	v_add_f32_e32 v199, v192, v248
	ds_read_b128 v[248:251], v157
	s_waitcnt lgkmcnt(7)
	v_mul_f32_e32 v217, v115, v217
	v_fmac_f32_e32 v217, v114, v216
	v_mul_f32_e32 v216, v113, v219
	v_fmac_f32_e32 v216, v112, v218
	v_add_f32_e32 v216, v217, v216
	v_add_f32_e32 v192, 0, v216
	ds_read_b128 v[216:219], v158
	s_waitcnt lgkmcnt(7)
	v_mul_f32_e32 v221, v95, v221
	v_fmac_f32_e32 v221, v94, v220
	v_mul_f32_e32 v220, v93, v223
	v_fmac_f32_e32 v220, v92, v222
	v_add_f32_e32 v220, v221, v220
	v_add_f32_e32 v192, v192, v220
	ds_read_b128 v[220:223], v159
	s_waitcnt lgkmcnt(7)
	v_mul_f32_e32 v225, v91, v225
	v_fmac_f32_e32 v225, v90, v224
	v_mul_f32_e32 v224, v89, v227
	v_fmac_f32_e32 v224, v88, v226
	v_add_f32_e32 v224, v225, v224
	v_add_f32_e32 v192, v192, v224
	ds_read_b128 v[224:227], v160
	s_waitcnt lgkmcnt(7)
	v_mul_f32_e32 v229, v87, v229
	v_fmac_f32_e32 v229, v86, v228
	v_mul_f32_e32 v228, v85, v231
	v_fmac_f32_e32 v228, v84, v230
	v_add_f32_e32 v228, v229, v228
	v_add_f32_e32 v192, v192, v228
	ds_read_b128 v[228:231], v161
	s_waitcnt lgkmcnt(7)
	v_mul_f32_e32 v233, v83, v233
	v_fmac_f32_e32 v233, v82, v232
	v_mul_f32_e32 v232, v81, v235
	v_fmac_f32_e32 v232, v80, v234
	v_add_f32_e32 v232, v233, v232
	v_add_f32_e32 v192, v192, v232
	ds_read_b128 v[232:235], v162
	s_waitcnt lgkmcnt(7)
	v_mul_f32_e32 v237, v79, v237
	v_fmac_f32_e32 v237, v78, v236
	v_mul_f32_e32 v236, v77, v239
	v_fmac_f32_e32 v236, v76, v238
	v_add_f32_e32 v236, v237, v236
	v_add_f32_e32 v192, v192, v236
	ds_read_b128 v[236:239], v163
	s_waitcnt lgkmcnt(7)
	v_mul_f32_e32 v241, v75, v241
	v_fmac_f32_e32 v241, v74, v240
	v_mul_f32_e32 v240, v73, v243
	v_fmac_f32_e32 v240, v72, v242
	v_add_f32_e32 v240, v241, v240
	v_add_f32_e32 v192, v192, v240
	ds_read_b128 v[240:243], v164
	s_waitcnt lgkmcnt(7)
	v_mul_f32_e32 v249, v71, v249
	v_fmac_f32_e32 v249, v70, v248
	v_mul_f32_e32 v248, v69, v251
	v_fmac_f32_e32 v248, v68, v250
	v_add_f32_e32 v248, v249, v248
	v_add_f32_e32 v200, v192, v248
	ds_read_b128 v[248:251], v165
	s_waitcnt lgkmcnt(7)
	v_mul_f32_e32 v217, v115, v217
	v_fmac_f32_e32 v217, v114, v216
	v_mul_f32_e32 v216, v113, v219
	v_fmac_f32_e32 v216, v112, v218
	v_add_f32_e32 v216, v217, v216
	v_add_f32_e32 v192, 0, v216
	ds_read_b128 v[216:219], v166
	s_waitcnt lgkmcnt(7)
	v_mul_f32_e32 v221, v95, v221
	v_fmac_f32_e32 v221, v94, v220
	v_mul_f32_e32 v220, v93, v223
	v_fmac_f32_e32 v220, v92, v222
	v_add_f32_e32 v220, v221, v220
	v_add_f32_e32 v192, v192, v220
	ds_read_b128 v[220:223], v167
	s_waitcnt lgkmcnt(7)
	v_mul_f32_e32 v225, v91, v225
	v_fmac_f32_e32 v225, v90, v224
	v_mul_f32_e32 v224, v89, v227
	v_fmac_f32_e32 v224, v88, v226
	v_add_f32_e32 v224, v225, v224
	v_add_f32_e32 v192, v192, v224
	ds_read_b128 v[224:227], v168
	s_waitcnt lgkmcnt(7)
	v_mul_f32_e32 v229, v87, v229
	v_fmac_f32_e32 v229, v86, v228
	v_mul_f32_e32 v228, v85, v231
	v_fmac_f32_e32 v228, v84, v230
	v_add_f32_e32 v228, v229, v228
	v_add_f32_e32 v192, v192, v228
	ds_read_b128 v[228:231], v169
	s_waitcnt lgkmcnt(7)
	v_mul_f32_e32 v233, v83, v233
	v_fmac_f32_e32 v233, v82, v232
	v_mul_f32_e32 v232, v81, v235
	v_fmac_f32_e32 v232, v80, v234
	v_add_f32_e32 v232, v233, v232
	v_add_f32_e32 v192, v192, v232
	ds_read_b128 v[232:235], v170
	s_waitcnt lgkmcnt(7)
	v_mul_f32_e32 v237, v79, v237
	v_fmac_f32_e32 v237, v78, v236
	v_mul_f32_e32 v236, v77, v239
	v_fmac_f32_e32 v236, v76, v238
	v_add_f32_e32 v236, v237, v236
	v_add_f32_e32 v192, v192, v236
	ds_read_b128 v[236:239], v171
	s_waitcnt lgkmcnt(7)
	v_mul_f32_e32 v241, v75, v241
	v_fmac_f32_e32 v241, v74, v240
	v_mul_f32_e32 v240, v73, v243
	v_fmac_f32_e32 v240, v72, v242
	v_add_f32_e32 v240, v241, v240
	v_add_f32_e32 v192, v192, v240
	ds_read_b128 v[240:243], v172
	s_waitcnt lgkmcnt(7)
	v_mul_f32_e32 v249, v71, v249
	v_fmac_f32_e32 v249, v70, v248
	v_mul_f32_e32 v248, v69, v251
	v_fmac_f32_e32 v248, v68, v250
	v_add_f32_e32 v248, v249, v248
	v_add_f32_e32 v201, v192, v248
	ds_read_b128 v[248:251], v173
	s_waitcnt lgkmcnt(7)
	v_mul_f32_e32 v217, v115, v217
	v_fmac_f32_e32 v217, v114, v216
	v_mul_f32_e32 v216, v113, v219
	v_fmac_f32_e32 v216, v112, v218
	v_add_f32_e32 v216, v217, v216
	v_add_f32_e32 v192, 0, v216
	ds_read_b128 v[216:219], v174
	s_waitcnt lgkmcnt(7)
	v_mul_f32_e32 v221, v95, v221
	v_fmac_f32_e32 v221, v94, v220
	v_mul_f32_e32 v220, v93, v223
	v_fmac_f32_e32 v220, v92, v222
	v_add_f32_e32 v220, v221, v220
	v_add_f32_e32 v192, v192, v220
	ds_read_b128 v[220:223], v175
	s_waitcnt lgkmcnt(7)
	v_mul_f32_e32 v225, v91, v225
	v_fmac_f32_e32 v225, v90, v224
	v_mul_f32_e32 v224, v89, v227
	v_fmac_f32_e32 v224, v88, v226
	v_add_f32_e32 v224, v225, v224
	v_add_f32_e32 v192, v192, v224
	ds_read_b128 v[224:227], v176
	s_waitcnt lgkmcnt(7)
	v_mul_f32_e32 v229, v87, v229
	v_fmac_f32_e32 v229, v86, v228
	v_mul_f32_e32 v228, v85, v231
	v_fmac_f32_e32 v228, v84, v230
	v_add_f32_e32 v228, v229, v228
	v_add_f32_e32 v192, v192, v228
	ds_read_b128 v[228:231], v177
	s_waitcnt lgkmcnt(7)
	v_mul_f32_e32 v233, v83, v233
	v_fmac_f32_e32 v233, v82, v232
	v_mul_f32_e32 v232, v81, v235
	v_fmac_f32_e32 v232, v80, v234
	v_add_f32_e32 v232, v233, v232
	v_add_f32_e32 v192, v192, v232
	ds_read_b128 v[232:235], v178
	s_waitcnt lgkmcnt(7)
	v_mul_f32_e32 v237, v79, v237
	v_fmac_f32_e32 v237, v78, v236
	v_mul_f32_e32 v236, v77, v239
	v_fmac_f32_e32 v236, v76, v238
	v_add_f32_e32 v236, v237, v236
	v_add_f32_e32 v192, v192, v236
	ds_read_b128 v[236:239], v179
	s_waitcnt lgkmcnt(7)
; #define LAS __attribute__((address_space(3)))
; DI float sigmoidf_(float x) { return __builtin_amdgcn_rcpf(1.0f + __expf(-x)); }
; DI float softplusf_(float x) { return fmaxf(x, 0.f) + log1pf(__expf(-fabsf(x))); }
; template <int MODE, bool SB  > DI void norm_phase(const Params& P, const Frame& F, int L, const void* src_, const float* gain, bool combine) {
;     ...
;                 for (int j = 0; j < 8; ++j) { const f32x4 w = *(const LAS f32x4*)(F.lds + (size_t)(q * D + 256 * j + 4 * F.lane) * 4); t += (v[j][0] * w[0] + v[j][1] * w[1]) + (v[j][2] * w[2] + v[j][3] * w[3]); }
;                 s[q] = t; if ((q & 3) == 3) asm volatile("" ::: "memory"); }
; #pragma unroll
;             for (int i = 0; i < 8; ++i) { const bool hi = (F.lane & 32) != 0; const float send = hi ? s[i] : s[i + 8], keep = hi ? s[i + 8] : s[i]; s[i] = keep + shx<32>(send); }
; #pragma unroll
;             for (int i = 0; i < 4; ++i) { const bool hi = (F.lane & 16) != 0; const float send = hi ? s[i] : s[i + 4], keep = hi ? s[i + 4] : s[i]; s[i] = keep + shx<16>(send); }
; #pragma unroll
;             for (int i = 0; i < 2; ++i) { const bool hi = (F.lane & 8) != 0; const float send = hi ? s[i] : s[i + 2], keep = hi ? s[i + 2] : s[i]; s[i] = keep + shx<8>(send); }
;             { const bool hi = (F.lane & 4) != 0; const float send = hi ? s[0] : s[1], keep = hi ? s[1] : s[0]; s[0] = keep + shx<4>(send); }
;             float mine = s[0]; mine += shx<2>(mine); mine += shx<1>(mine);
;             if ((F.lane & 3) == 0) { const int gi = ((F.lane >> 5) & 1) * 8 + ((F.lane >> 4) & 1) * 4 + ((F.lane >> 3) & 1) * 2 + ((F.lane >> 2) & 1), h = gi & 3; float r;
;                 if (gi < 4) r = sigmoidf_(mine);
;                 else if (gi < 8) r = -__expf(P.in[I_DN_A_LOG][L * 4 + h]) * softplusf_(mine + P.in[I_DN_DT_BIAS][L * 4 + h]);
;                 else if (gi < 12) r = mine + P.in[I_ML_I_BIAS][L * 4 + h];
;                 else r = -softplusf_(-(mine + P.in[I_ML_F_BIAS][L * 4 + h]));
;                 ((float*)(ws + WS_GD))[(size_t)row * 16 + gi] = r; }
	v_mul_f32_e32 v241, v75, v241
	v_fmac_f32_e32 v241, v74, v240
	v_mul_f32_e32 v240, v73, v243
	v_fmac_f32_e32 v240, v72, v242
	v_add_f32_e32 v240, v241, v240
	v_add_f32_e32 v192, v192, v240
	ds_read_b128 v[240:243], v180
	s_waitcnt lgkmcnt(7)
	v_mul_f32_e32 v249, v71, v249
	v_fmac_f32_e32 v249, v70, v248
	v_mul_f32_e32 v248, v69, v251
	v_fmac_f32_e32 v248, v68, v250
	v_add_f32_e32 v248, v249, v248
	v_add_f32_e32 v202, v192, v248
	ds_read_b128 v[64:67], v181
	s_waitcnt lgkmcnt(7)
	v_mul_f32_e32 v217, v115, v217
	v_fmac_f32_e32 v217, v114, v216
	v_mul_f32_e32 v216, v113, v219
	v_fmac_f32_e32 v216, v112, v218
	v_add_f32_e32 v216, v217, v216
	v_add_f32_e32 v112, 0, v216
	s_waitcnt lgkmcnt(6)
	v_mul_f32_e32 v221, v95, v221
	v_fmac_f32_e32 v221, v94, v220
	v_mul_f32_e32 v220, v93, v223
	v_fmac_f32_e32 v220, v92, v222
	v_add_f32_e32 v220, v221, v220
	v_add_f32_e32 v92, v112, v220
	s_waitcnt lgkmcnt(5)
	v_mul_f32_e32 v225, v91, v225
	v_fmac_f32_e32 v225, v90, v224
	v_mul_f32_e32 v224, v89, v227
	v_fmac_f32_e32 v224, v88, v226
	v_add_f32_e32 v224, v225, v224
	v_add_f32_e32 v88, v92, v224
	s_waitcnt lgkmcnt(4)
	v_mul_f32_e32 v229, v87, v229
	v_fmac_f32_e32 v229, v86, v228
	v_mul_f32_e32 v228, v85, v231
	v_fmac_f32_e32 v228, v84, v230
	v_add_f32_e32 v228, v229, v228
	v_add_f32_e32 v84, v88, v228
	s_waitcnt lgkmcnt(3)
	v_mul_f32_e32 v233, v83, v233
	v_fmac_f32_e32 v233, v82, v232
	v_mul_f32_e32 v232, v81, v235
	v_fmac_f32_e32 v232, v80, v234
	v_add_f32_e32 v232, v233, v232
	v_add_f32_e32 v80, v84, v232
	s_waitcnt lgkmcnt(2)
	v_mul_f32_e32 v237, v79, v237
	v_fmac_f32_e32 v237, v78, v236
	v_mul_f32_e32 v236, v77, v239
	v_fmac_f32_e32 v236, v76, v238
	v_add_f32_e32 v236, v237, v236
	v_add_f32_e32 v76, v80, v236
	s_waitcnt lgkmcnt(1)
	v_mul_f32_e32 v241, v75, v241
	v_fmac_f32_e32 v241, v74, v240
	v_mul_f32_e32 v240, v73, v243
	v_fmac_f32_e32 v240, v72, v242
	v_add_f32_e32 v240, v241, v240
	v_add_f32_e32 v72, v76, v240
	s_waitcnt lgkmcnt(0)
	v_mul_f32_e32 v65, v71, v65
	v_fmac_f32_e32 v65, v70, v64
	v_mul_f32_e32 v64, v69, v67
	v_fmac_f32_e32 v64, v68, v66
	v_add_f32_e32 v64, v65, v64
	v_cndmask_b32_e64 v65, v111, v196, s[4:5]
	ds_bpermute_b32 v65, v116, v65
	v_cndmask_b32_e64 v66, v196, v111, s[4:5]
	v_cndmask_b32_e64 v67, v197, v188, s[4:5]
	v_cndmask_b32_e64 v68, v198, v189, s[4:5]
	v_cndmask_b32_e64 v69, v199, v190, s[4:5]
	s_waitcnt lgkmcnt(0)
	v_add_f32_e32 v65, v66, v65
	v_cndmask_b32_e64 v66, v188, v197, s[4:5]
	ds_bpermute_b32 v66, v116, v66
	v_cndmask_b32_e64 v70, v200, v191, s[4:5]
	v_cndmask_b32_e64 v71, v201, v193, s[4:5]
	v_add_f32_e32 v64, v72, v64
	v_cndmask_b32_e64 v72, v202, v194, s[4:5]
	s_waitcnt lgkmcnt(0)
	v_add_f32_e32 v66, v67, v66
	v_cndmask_b32_e64 v67, v189, v198, s[4:5]
	ds_bpermute_b32 v67, v116, v67
	s_waitcnt lgkmcnt(0)
	v_add_f32_e32 v67, v68, v67
	v_cndmask_b32_e64 v68, v190, v199, s[4:5]
	ds_bpermute_b32 v68, v116, v68
	s_waitcnt lgkmcnt(0)
	v_add_f32_e32 v68, v69, v68
	v_cndmask_b32_e64 v69, v191, v200, s[4:5]
	ds_bpermute_b32 v69, v116, v69
	s_waitcnt lgkmcnt(0)
	v_add_f32_e32 v69, v70, v69
	v_cndmask_b32_e64 v70, v193, v201, s[4:5]
	ds_bpermute_b32 v70, v116, v70
	s_waitcnt lgkmcnt(0)
	v_add_f32_e32 v70, v71, v70
	v_cndmask_b32_e64 v71, v194, v202, s[4:5]
	ds_bpermute_b32 v71, v116, v71
	s_waitcnt lgkmcnt(0)
	v_add_f32_e32 v71, v72, v71
	v_cndmask_b32_e64 v72, v195, v64, s[4:5]
	ds_bpermute_b32 v72, v116, v72
	v_cndmask_b32_e64 v64, v64, v195, s[4:5]
	s_waitcnt lgkmcnt(0)
	v_add_f32_e32 v64, v64, v72
	v_cndmask_b32_e64 v72, v65, v69, s[8:9]
	v_cndmask_b32_e64 v65, v69, v65, s[8:9]
	ds_swizzle_b32 v69, v72 offset:swizzle(SWAP,16)
	s_waitcnt lgkmcnt(0)
	v_add_f32_e32 v65, v65, v69
	v_cndmask_b32_e64 v69, v66, v70, s[8:9]
	ds_swizzle_b32 v69, v69 offset:swizzle(SWAP,16)
	v_cndmask_b32_e64 v66, v70, v66, s[8:9]
	s_waitcnt lgkmcnt(0)
	v_add_f32_e32 v66, v66, v69
	v_cndmask_b32_e64 v69, v67, v71, s[8:9]
	ds_swizzle_b32 v69, v69 offset:swizzle(SWAP,16)
	v_cndmask_b32_e64 v67, v71, v67, s[8:9]
	s_waitcnt lgkmcnt(0)
	v_add_f32_e32 v67, v67, v69
	v_cndmask_b32_e64 v69, v68, v64, s[8:9]
	v_cndmask_b32_e64 v64, v64, v68, s[8:9]
	ds_swizzle_b32 v68, v69 offset:swizzle(SWAP,16)
	s_waitcnt lgkmcnt(0)
	v_add_f32_e32 v64, v64, v68
	v_cndmask_b32_e64 v68, v65, v67, s[10:11]
	v_cndmask_b32_e64 v65, v67, v65, s[10:11]
	ds_swizzle_b32 v67, v68 offset:swizzle(SWAP,8)
	s_waitcnt lgkmcnt(0)
	v_add_f32_e32 v65, v65, v67
	v_cndmask_b32_e64 v67, v66, v64, s[10:11]
	v_cndmask_b32_e64 v64, v64, v66, s[10:11]
	ds_swizzle_b32 v66, v67 offset:swizzle(SWAP,8)
	s_waitcnt lgkmcnt(0)
	v_add_f32_e32 v64, v64, v66
	v_cndmask_b32_e64 v66, v65, v64, s[12:13]
	v_cndmask_b32_e64 v64, v64, v65, s[12:13]
	ds_swizzle_b32 v65, v66 offset:swizzle(SWAP,4)
	s_waitcnt lgkmcnt(0)
	v_add_f32_e32 v64, v64, v65
	s_nop 1
	v_add_f32_dpp v64, v64, v64 quad_perm:[2,3,0,1] row_mask:0xf bank_mask:0xf bound_ctrl:1
	s_nop 1
	v_mov_b32_dpp v65, v64 quad_perm:[1,0,3,2] row_mask:0xf bank_mask:0xf bound_ctrl:1
	s_and_saveexec_b64 s[20:21], s[14:15]
	s_cbranch_execz .LBB0_82
	v_add_f32_e32 v65, v64, v65
	s_and_saveexec_b64 s[24:25], s[16:17]
	s_xor_b64 s[24:25], exec, s[24:25]
	s_cbranch_execz .LBB0_94
	s_and_saveexec_b64 s[26:27], s[6:7]
	s_xor_b64 s[26:27], exec, s[26:27]
	s_cbranch_execz .LBB0_91
	s_and_saveexec_b64 s[28:29], s[18:19]
	s_xor_b64 s[28:29], exec, s[28:29]
	s_cbranch_execz .LBB0_88
	global_load_dword v64, v[98:99], off
	s_waitcnt vmcnt(0)
	v_add_f32_e32 v64, v65, v64
